# v94 + phase E final epilogue: counted vmcnt ladder (7..0) over the 8 gate loads
# baseline (speedup 1.0000x reference)
.LBB0_3874:
	v_mov_b32_e32 v130, v247
	v_mov_b32_e32 v131, v246
	s_or_b32 s0, s17, s47
	v_pk_mul_f32 v[126:127], v[126:127], s[88:89] op_sel_hi:[1,0]
	v_lshl_add_u32 v158, v130, 4, s0
	v_ashrrev_i32_e32 v159, 31, v158
	v_add_u32_e32 v174, s50, v131
	v_lshl_add_u64 v[130:131], s[10:11], 0, v[158:159]
	v_mad_i64_i32 v[132:133], s[20:21], v174, s64, v[130:131]
	v_add_co_u32_e32 v132, vcc, 0x1000, v132
	v_add_u32_e32 v172, 16, v174
	s_nop 0
	v_addc_co_u32_e32 v133, vcc, 0, v133, vcc
	v_mad_i64_i32 v[134:135], s[20:21], v172, s64, v[130:131]
	v_add_co_u32_e32 v134, vcc, 0x1000, v134
	v_add_u32_e32 v170, 32, v174
	s_nop 0
	v_addc_co_u32_e32 v135, vcc, 0, v135, vcc
	global_load_dwordx4 v[176:179], v[132:133], off
	global_load_dwordx4 v[154:157], v[134:135], off
	v_mad_i64_i32 v[132:133], s[20:21], v170, s64, v[130:131]
	v_add_co_u32_e32 v132, vcc, 0x1000, v132
	v_add_u32_e32 v168, 48, v174
	s_nop 0
	v_addc_co_u32_e32 v133, vcc, 0, v133, vcc
	v_mad_i64_i32 v[134:135], s[20:21], v168, s64, v[130:131]
	v_add_co_u32_e32 v134, vcc, 0x1000, v134
	v_add_u32_e32 v166, 0x80, v174
	s_nop 0
	v_addc_co_u32_e32 v135, vcc, 0, v135, vcc
	global_load_dwordx4 v[150:153], v[132:133], off
	global_load_dwordx4 v[146:149], v[134:135], off
	v_mad_i64_i32 v[132:133], s[20:21], v166, s64, v[130:131]
	v_add_co_u32_e32 v132, vcc, 0x1000, v132
	v_add_u32_e32 v164, 0x90, v174
	s_nop 0
	v_addc_co_u32_e32 v133, vcc, 0, v133, vcc
	v_mad_i64_i32 v[134:135], s[20:21], v164, s64, v[130:131]
	v_add_co_u32_e32 v134, vcc, 0x1000, v134
	v_add_u32_e32 v162, 0xa0, v174
	s_nop 0
	v_addc_co_u32_e32 v135, vcc, 0, v135, vcc
	global_load_dwordx4 v[142:145], v[132:133], off
	global_load_dwordx4 v[138:141], v[134:135], off
	v_mad_i64_i32 v[132:133], s[20:21], v162, s64, v[130:131]
	v_add_co_u32_e32 v132, vcc, 0x1000, v132
	v_add_u32_e32 v160, 0xb0, v174
	s_nop 0
	v_addc_co_u32_e32 v133, vcc, 0, v133, vcc
	v_mad_i64_i32 v[130:131], s[20:21], v160, s64, v[130:131]
	v_add_co_u32_e32 v130, vcc, 0x1000, v130
	v_pk_mul_f32 v[128:129], v[128:129], s[88:89] op_sel_hi:[1,0]
	s_nop 0
	v_addc_co_u32_e32 v131, vcc, 0, v131, vcc
	global_load_dwordx4 v[134:137], v[132:133], off
	s_nop 0
	global_load_dwordx4 v[130:133], v[130:131], off
	v_pk_mul_f32 v[124:125], v[124:125], s[88:89] op_sel_hi:[1,0]
	v_pk_mul_f32 v[118:119], v[118:119], s[88:89] op_sel_hi:[1,0]
	v_pk_mul_f32 v[114:115], v[114:115], s[88:89] op_sel_hi:[1,0]
	v_pk_mul_f32 v[120:121], v[120:121], s[88:89] op_sel_hi:[1,0]
	v_pk_mul_f32 v[116:117], v[116:117], s[88:89] op_sel_hi:[1,0]
	v_ashrrev_i32_e32 v175, 31, v174
	v_pk_mul_f32 v[110:111], v[110:111], s[88:89] op_sel_hi:[1,0]
	v_pk_mul_f32 v[112:113], v[112:113], s[88:89] op_sel_hi:[1,0]
	v_pk_mul_f32 v[108:109], v[108:109], s[88:89] op_sel_hi:[1,0]
	v_pk_mul_f32 v[102:103], v[102:103], s[88:89] op_sel_hi:[1,0]
	v_pk_mul_f32 v[98:99], v[98:99], s[88:89] op_sel_hi:[1,0]
	v_pk_mul_f32 v[104:105], v[104:105], s[88:89] op_sel_hi:[1,0]
	v_pk_mul_f32 v[100:101], v[100:101], s[88:89] op_sel_hi:[1,0]
	v_ashrrev_i32_e32 v173, 31, v172
	v_pk_mul_f32 v[94:95], v[94:95], s[88:89] op_sel_hi:[1,0]
	v_pk_mul_f32 v[96:97], v[96:97], s[88:89] op_sel_hi:[1,0]
	v_pk_mul_f32 v[92:93], v[92:93], s[88:89] op_sel_hi:[1,0]
	v_pk_mul_f32 v[86:87], v[86:87], s[88:89] op_sel_hi:[1,0]
	v_pk_mul_f32 v[82:83], v[82:83], s[88:89] op_sel_hi:[1,0]
	v_pk_mul_f32 v[88:89], v[88:89], s[88:89] op_sel_hi:[1,0]
	v_pk_mul_f32 v[84:85], v[84:85], s[88:89] op_sel_hi:[1,0]
	v_ashrrev_i32_e32 v171, 31, v170
	v_pk_mul_f32 v[78:79], v[78:79], s[88:89] op_sel_hi:[1,0]
	v_pk_mul_f32 v[80:81], v[80:81], s[88:89] op_sel_hi:[1,0]
	v_pk_mul_f32 v[76:77], v[76:77], s[88:89] op_sel_hi:[1,0]
	v_pk_mul_f32 v[70:71], v[70:71], s[88:89] op_sel_hi:[1,0]
	v_pk_mul_f32 v[66:67], v[66:67], s[88:89] op_sel_hi:[1,0]
	v_pk_mul_f32 v[72:73], v[72:73], s[88:89] op_sel_hi:[1,0]
	v_pk_mul_f32 v[68:69], v[68:69], s[88:89] op_sel_hi:[1,0]
	v_ashrrev_i32_e32 v169, 31, v168
	v_pk_mul_f32 v[62:63], v[62:63], s[88:89] op_sel_hi:[1,0]
	v_pk_mul_f32 v[64:65], v[64:65], s[88:89] op_sel_hi:[1,0]
	s_nop 0
	s_nop 0
	s_waitcnt vmcnt(7)
	v_cvt_f32_ubyte0_e32 v180, v176
	v_cvt_f32_ubyte1_e32 v181, v176
	v_cvt_f32_ubyte2_e32 v182, v176
	v_cvt_f32_ubyte3_e32 v183, v176
	v_cvt_f32_ubyte0_e32 v184, v177
	v_cvt_f32_ubyte1_e32 v185, v177
	v_cvt_f32_ubyte2_e32 v186, v177
	v_cvt_f32_ubyte3_e32 v187, v177
	v_pk_mul_f32 v[176:177], v[122:123], s[88:89] op_sel_hi:[1,0]
	v_mul_f32_e32 v122, v126, v180
	v_mul_f32_e32 v123, v127, v181
	v_mul_f32_e32 v122, 0x41800000, v122
	v_mul_f32_e32 v123, 0x41800000, v123
	v_mul_f32_e32 v126, v128, v182
	v_med3_f32 v128, v122, s76, v237
	v_med3_f32 v123, v123, s76, v237
	v_mov_b32_e32 v122, v1
	v_cvt_pk_fp8_f32 v122, v128, v123
	v_mul_f32_e32 v127, v129, v183
	v_mul_f32_e32 v126, 0x41800000, v126
	v_mul_f32_e32 v123, 0x41800000, v127
	v_med3_f32 v126, v126, s76, v237
	v_med3_f32 v123, v123, s76, v237
	v_cvt_pk_fp8_f32 v122, v126, v123 op_sel:[0,0,1]
	v_mul_f32_e32 v123, v176, v184
	v_mul_f32_e32 v126, v177, v185
	v_mul_f32_e32 v123, 0x41800000, v123
	v_mul_f32_e32 v126, 0x41800000, v126
	v_med3_f32 v127, v123, s76, v237
	v_med3_f32 v126, v126, s76, v237
	v_mov_b32_e32 v123, v1
	v_cvt_pk_fp8_f32 v123, v127, v126
	v_mul_f32_e32 v124, v124, v186
	v_mul_f32_e32 v125, v125, v187
	v_mul_f32_e32 v124, 0x41800000, v124
	v_mul_f32_e32 v125, 0x41800000, v125
	v_med3_f32 v124, v124, s76, v237
	v_med3_f32 v125, v125, s76, v237
	v_cvt_pk_fp8_f32 v123, v124, v125 op_sel:[0,0,1]
	v_cvt_f32_ubyte0_e32 v124, v178
	v_cvt_f32_ubyte1_e32 v125, v178
	v_cvt_f32_ubyte0_e32 v128, v179
	v_cvt_f32_ubyte1_e32 v129, v179
	v_mul_f32_e32 v118, v118, v124
	v_mul_f32_e32 v119, v119, v125
	v_mul_f32_e32 v114, v114, v128
	v_mul_f32_e32 v115, v115, v129
	v_mul_f32_e32 v118, 0x41800000, v118
	v_mul_f32_e32 v119, 0x41800000, v119
	v_mul_f32_e32 v114, 0x41800000, v114
	v_mul_f32_e32 v115, 0x41800000, v115
	v_med3_f32 v118, v118, s76, v237
	v_med3_f32 v119, v119, s76, v237
	v_mov_b32_e32 v124, v1
	v_med3_f32 v114, v114, s76, v237
	v_med3_f32 v115, v115, s76, v237
	v_mov_b32_e32 v125, v1
	v_cvt_f32_ubyte2_e32 v126, v178
	v_cvt_f32_ubyte3_e32 v127, v178
	v_cvt_f32_ubyte2_e32 v176, v179
	v_cvt_f32_ubyte3_e32 v177, v179
	v_cvt_pk_fp8_f32 v124, v118, v119
	v_cvt_pk_fp8_f32 v125, v114, v115
	v_mul_f32_e32 v120, v120, v126
	v_mul_f32_e32 v121, v121, v127
	v_mul_f32_e32 v116, v116, v176
	v_mul_f32_e32 v117, v117, v177
	v_mul_f32_e32 v120, 0x41800000, v120
	v_mul_f32_e32 v118, 0x41800000, v121
	v_mul_f32_e32 v116, 0x41800000, v116
	v_mul_f32_e32 v114, 0x41800000, v117
	v_med3_f32 v119, v120, s76, v237
	v_med3_f32 v118, v118, s76, v237
	v_med3_f32 v115, v116, s76, v237
	v_med3_f32 v114, v114, s76, v237
	v_cvt_pk_fp8_f32 v124, v119, v118 op_sel:[0,0,1]
	v_cvt_pk_fp8_f32 v125, v115, v114 op_sel:[0,0,1]
	v_lshlrev_b64 v[114:115], 11, v[174:175]
	v_lshl_add_u64 v[114:115], s[12:13], 0, v[114:115]
	v_lshl_add_u64 v[114:115], v[114:115], 0, v[158:159]
	s_waitcnt vmcnt(6)
	v_cvt_f32_ubyte0_e32 v116, v154
	v_cvt_f32_ubyte1_e32 v117, v154
	global_store_dwordx4 v[114:115], v[122:125], off
	v_pk_mul_f32 v[114:115], v[106:107], s[88:89] op_sel_hi:[1,0]
	v_mul_f32_e32 v106, v110, v116
	v_mul_f32_e32 v107, v111, v117
	v_cvt_f32_ubyte2_e32 v118, v154
	v_mul_f32_e32 v106, 0x41800000, v106
	v_mul_f32_e32 v107, 0x41800000, v107
	v_mul_f32_e32 v110, v112, v118
	v_med3_f32 v112, v106, s76, v237
	v_med3_f32 v107, v107, s76, v237
	v_mov_b32_e32 v106, v1
	v_cvt_f32_ubyte3_e32 v119, v154
	v_cvt_pk_fp8_f32 v106, v112, v107
	v_mul_f32_e32 v111, v113, v119
	v_mul_f32_e32 v110, 0x41800000, v110
	v_mul_f32_e32 v107, 0x41800000, v111
	v_cvt_f32_ubyte0_e32 v120, v155
	v_cvt_f32_ubyte1_e32 v121, v155
	v_med3_f32 v110, v110, s76, v237
	v_med3_f32 v107, v107, s76, v237
	v_cvt_pk_fp8_f32 v106, v110, v107 op_sel:[0,0,1]
	v_mul_f32_e32 v107, v114, v120
	v_mul_f32_e32 v110, v115, v121
	v_mul_f32_e32 v107, 0x41800000, v107
	v_mul_f32_e32 v110, 0x41800000, v110
	v_med3_f32 v111, v107, s76, v237
	v_med3_f32 v110, v110, s76, v237
	v_mov_b32_e32 v107, v1
	v_cvt_f32_ubyte2_e32 v122, v155
	v_cvt_f32_ubyte3_e32 v123, v155
	v_cvt_pk_fp8_f32 v107, v111, v110
	v_mul_f32_e32 v108, v108, v122
	v_mul_f32_e32 v109, v109, v123
	v_mul_f32_e32 v108, 0x41800000, v108
	v_mul_f32_e32 v109, 0x41800000, v109
	v_med3_f32 v108, v108, s76, v237
	v_med3_f32 v109, v109, s76, v237
	v_cvt_pk_fp8_f32 v107, v108, v109 op_sel:[0,0,1]
	v_cvt_f32_ubyte0_e32 v108, v156
	v_cvt_f32_ubyte1_e32 v109, v156
	v_cvt_f32_ubyte0_e32 v112, v157
	v_cvt_f32_ubyte1_e32 v113, v157
	v_mul_f32_e32 v102, v102, v108
	v_mul_f32_e32 v103, v103, v109
	v_mul_f32_e32 v98, v98, v112
	v_mul_f32_e32 v99, v99, v113
	v_mul_f32_e32 v102, 0x41800000, v102
	v_mul_f32_e32 v103, 0x41800000, v103
	v_mul_f32_e32 v98, 0x41800000, v98
	v_mul_f32_e32 v99, 0x41800000, v99
	v_med3_f32 v102, v102, s76, v237
	v_med3_f32 v103, v103, s76, v237
	v_mov_b32_e32 v108, v1
	v_med3_f32 v98, v98, s76, v237
	v_med3_f32 v99, v99, s76, v237
	v_mov_b32_e32 v109, v1
	v_cvt_f32_ubyte2_e32 v110, v156
	v_cvt_f32_ubyte3_e32 v111, v156
	v_cvt_f32_ubyte2_e32 v114, v157
	v_cvt_f32_ubyte3_e32 v115, v157
	v_cvt_pk_fp8_f32 v108, v102, v103
	v_cvt_pk_fp8_f32 v109, v98, v99
	v_mul_f32_e32 v104, v104, v110
	v_mul_f32_e32 v105, v105, v111
	v_mul_f32_e32 v100, v100, v114
	v_mul_f32_e32 v101, v101, v115
	v_mul_f32_e32 v104, 0x41800000, v104
	v_mul_f32_e32 v102, 0x41800000, v105
	v_mul_f32_e32 v100, 0x41800000, v100
	v_mul_f32_e32 v98, 0x41800000, v101
	v_med3_f32 v103, v104, s76, v237
	v_med3_f32 v102, v102, s76, v237
	v_med3_f32 v99, v100, s76, v237
	v_med3_f32 v98, v98, s76, v237
	v_cvt_pk_fp8_f32 v108, v103, v102 op_sel:[0,0,1]
	v_cvt_pk_fp8_f32 v109, v99, v98 op_sel:[0,0,1]
	v_lshlrev_b64 v[98:99], 11, v[172:173]
	v_lshl_add_u64 v[98:99], s[12:13], 0, v[98:99]
	v_lshl_add_u64 v[98:99], v[98:99], 0, v[158:159]
	s_waitcnt vmcnt(5)
	v_cvt_f32_ubyte0_e32 v100, v150
	v_cvt_f32_ubyte1_e32 v101, v150
	global_store_dwordx4 v[98:99], v[106:109], off
	v_pk_mul_f32 v[98:99], v[90:91], s[88:89] op_sel_hi:[1,0]
	v_mul_f32_e32 v90, v94, v100
	v_mul_f32_e32 v91, v95, v101
	v_cvt_f32_ubyte2_e32 v102, v150
	v_mul_f32_e32 v90, 0x41800000, v90
	v_mul_f32_e32 v91, 0x41800000, v91
	v_mul_f32_e32 v94, v96, v102
	v_med3_f32 v96, v90, s76, v237
	v_med3_f32 v91, v91, s76, v237
	v_mov_b32_e32 v90, v1
	v_cvt_f32_ubyte3_e32 v103, v150
	v_cvt_pk_fp8_f32 v90, v96, v91
	v_mul_f32_e32 v95, v97, v103
	v_mul_f32_e32 v94, 0x41800000, v94
	v_mul_f32_e32 v91, 0x41800000, v95
	v_cvt_f32_ubyte0_e32 v104, v151
	v_cvt_f32_ubyte1_e32 v105, v151
	v_med3_f32 v94, v94, s76, v237
	v_med3_f32 v91, v91, s76, v237
	v_cvt_pk_fp8_f32 v90, v94, v91 op_sel:[0,0,1]
	v_mul_f32_e32 v91, v98, v104
	v_mul_f32_e32 v94, v99, v105
	v_mul_f32_e32 v91, 0x41800000, v91
	v_mul_f32_e32 v94, 0x41800000, v94
	v_med3_f32 v95, v91, s76, v237
	v_med3_f32 v94, v94, s76, v237
	v_mov_b32_e32 v91, v1
	v_cvt_f32_ubyte2_e32 v106, v151
	v_cvt_f32_ubyte3_e32 v107, v151
	v_cvt_pk_fp8_f32 v91, v95, v94
	v_mul_f32_e32 v92, v92, v106
	v_mul_f32_e32 v93, v93, v107
	v_mul_f32_e32 v92, 0x41800000, v92
	v_mul_f32_e32 v93, 0x41800000, v93
	v_med3_f32 v92, v92, s76, v237
	v_med3_f32 v93, v93, s76, v237
	v_cvt_pk_fp8_f32 v91, v92, v93 op_sel:[0,0,1]
	v_cvt_f32_ubyte0_e32 v92, v152
	v_cvt_f32_ubyte1_e32 v93, v152
	v_cvt_f32_ubyte0_e32 v96, v153
	v_cvt_f32_ubyte1_e32 v97, v153
	v_mul_f32_e32 v86, v86, v92
	v_mul_f32_e32 v87, v87, v93
	v_mul_f32_e32 v82, v82, v96
	v_mul_f32_e32 v83, v83, v97
	v_mul_f32_e32 v86, 0x41800000, v86
	v_mul_f32_e32 v87, 0x41800000, v87
	v_mul_f32_e32 v82, 0x41800000, v82
	v_mul_f32_e32 v83, 0x41800000, v83
	v_med3_f32 v86, v86, s76, v237
	v_med3_f32 v87, v87, s76, v237
	v_mov_b32_e32 v92, v1
	v_med3_f32 v82, v82, s76, v237
	v_med3_f32 v83, v83, s76, v237
	v_mov_b32_e32 v93, v1
	v_cvt_f32_ubyte2_e32 v94, v152
	v_cvt_f32_ubyte3_e32 v95, v152
	v_cvt_f32_ubyte2_e32 v98, v153
	v_cvt_f32_ubyte3_e32 v99, v153
	v_cvt_pk_fp8_f32 v92, v86, v87
	v_cvt_pk_fp8_f32 v93, v82, v83
	v_mul_f32_e32 v88, v88, v94
	v_mul_f32_e32 v89, v89, v95
	v_mul_f32_e32 v84, v84, v98
	v_mul_f32_e32 v85, v85, v99
	v_mul_f32_e32 v88, 0x41800000, v88
	v_mul_f32_e32 v86, 0x41800000, v89
	v_mul_f32_e32 v84, 0x41800000, v84
	v_mul_f32_e32 v82, 0x41800000, v85
	v_med3_f32 v87, v88, s76, v237
	v_med3_f32 v86, v86, s76, v237
	v_med3_f32 v83, v84, s76, v237
	v_med3_f32 v82, v82, s76, v237
	v_cvt_pk_fp8_f32 v92, v87, v86 op_sel:[0,0,1]
	v_cvt_pk_fp8_f32 v93, v83, v82 op_sel:[0,0,1]
	v_lshlrev_b64 v[82:83], 11, v[170:171]
	v_lshl_add_u64 v[82:83], s[12:13], 0, v[82:83]
	v_lshl_add_u64 v[82:83], v[82:83], 0, v[158:159]
	s_waitcnt vmcnt(4)
	v_cvt_f32_ubyte0_e32 v84, v146
	v_cvt_f32_ubyte1_e32 v85, v146
	global_store_dwordx4 v[82:83], v[90:93], off
	v_pk_mul_f32 v[82:83], v[74:75], s[88:89] op_sel_hi:[1,0]
	v_mul_f32_e32 v74, v78, v84
	v_mul_f32_e32 v75, v79, v85
	v_cvt_f32_ubyte2_e32 v86, v146
	v_mul_f32_e32 v74, 0x41800000, v74
	v_mul_f32_e32 v75, 0x41800000, v75
	v_mul_f32_e32 v78, v80, v86
	v_med3_f32 v80, v74, s76, v237
	v_med3_f32 v75, v75, s76, v237
	v_mov_b32_e32 v74, v1
	v_cvt_f32_ubyte3_e32 v87, v146
	v_cvt_pk_fp8_f32 v74, v80, v75
	v_mul_f32_e32 v79, v81, v87
	v_mul_f32_e32 v78, 0x41800000, v78
	v_mul_f32_e32 v75, 0x41800000, v79
	v_cvt_f32_ubyte0_e32 v88, v147
	v_cvt_f32_ubyte1_e32 v89, v147
	v_med3_f32 v78, v78, s76, v237
	v_med3_f32 v75, v75, s76, v237
	v_cvt_pk_fp8_f32 v74, v78, v75 op_sel:[0,0,1]
	v_mul_f32_e32 v75, v82, v88
	v_mul_f32_e32 v78, v83, v89
	v_mul_f32_e32 v75, 0x41800000, v75
	v_mul_f32_e32 v78, 0x41800000, v78
	v_med3_f32 v79, v75, s76, v237
	v_med3_f32 v78, v78, s76, v237
	v_mov_b32_e32 v75, v1
	v_cvt_f32_ubyte2_e32 v90, v147
	v_cvt_f32_ubyte3_e32 v91, v147
	v_cvt_pk_fp8_f32 v75, v79, v78
	v_mul_f32_e32 v76, v76, v90
	v_mul_f32_e32 v77, v77, v91
	v_mul_f32_e32 v76, 0x41800000, v76
	v_mul_f32_e32 v77, 0x41800000, v77
	v_med3_f32 v76, v76, s76, v237
	v_med3_f32 v77, v77, s76, v237
	v_cvt_pk_fp8_f32 v75, v76, v77 op_sel:[0,0,1]
	v_cvt_f32_ubyte0_e32 v76, v148
	v_cvt_f32_ubyte1_e32 v77, v148
	v_cvt_f32_ubyte0_e32 v80, v149
	v_cvt_f32_ubyte1_e32 v81, v149
	v_mul_f32_e32 v70, v70, v76
	v_mul_f32_e32 v71, v71, v77
	v_mul_f32_e32 v66, v66, v80
	v_mul_f32_e32 v67, v67, v81
	v_mul_f32_e32 v70, 0x41800000, v70
	v_mul_f32_e32 v71, 0x41800000, v71
	v_mul_f32_e32 v66, 0x41800000, v66
	v_mul_f32_e32 v67, 0x41800000, v67
	v_med3_f32 v70, v70, s76, v237
	v_med3_f32 v71, v71, s76, v237
	v_mov_b32_e32 v76, v1
	v_med3_f32 v66, v66, s76, v237
	v_med3_f32 v67, v67, s76, v237
	v_mov_b32_e32 v77, v1
	v_cvt_f32_ubyte2_e32 v78, v148
	v_cvt_f32_ubyte3_e32 v79, v148
	v_cvt_f32_ubyte2_e32 v82, v149
	v_cvt_f32_ubyte3_e32 v83, v149
	v_cvt_pk_fp8_f32 v76, v70, v71
	v_cvt_pk_fp8_f32 v77, v66, v67
	v_mul_f32_e32 v72, v72, v78
	v_mul_f32_e32 v73, v73, v79
	v_mul_f32_e32 v68, v68, v82
	v_mul_f32_e32 v69, v69, v83
	v_mul_f32_e32 v72, 0x41800000, v72
	v_mul_f32_e32 v70, 0x41800000, v73
	v_mul_f32_e32 v68, 0x41800000, v68
	v_mul_f32_e32 v66, 0x41800000, v69
	v_med3_f32 v71, v72, s76, v237
	v_med3_f32 v70, v70, s76, v237
	v_med3_f32 v67, v68, s76, v237
	v_med3_f32 v66, v66, s76, v237
	v_cvt_pk_fp8_f32 v76, v71, v70 op_sel:[0,0,1]
	v_cvt_pk_fp8_f32 v77, v67, v66 op_sel:[0,0,1]
	v_lshlrev_b64 v[66:67], 11, v[168:169]
	v_lshl_add_u64 v[66:67], s[12:13], 0, v[66:67]
	v_lshl_add_u64 v[66:67], v[66:67], 0, v[158:159]
	s_waitcnt vmcnt(3)
	v_cvt_f32_ubyte0_e32 v68, v142
	v_cvt_f32_ubyte1_e32 v69, v142
	global_store_dwordx4 v[66:67], v[74:77], off
	v_pk_mul_f32 v[66:67], v[58:59], s[88:89] op_sel_hi:[1,0]
	v_mul_f32_e32 v58, v62, v68
	v_mul_f32_e32 v59, v63, v69
	v_cvt_f32_ubyte2_e32 v70, v142
	v_mul_f32_e32 v58, 0x41800000, v58
	v_mul_f32_e32 v59, 0x41800000, v59
	v_mul_f32_e32 v62, v64, v70
	v_med3_f32 v64, v58, s76, v237
	v_med3_f32 v59, v59, s76, v237
	v_mov_b32_e32 v58, v1
	v_cvt_f32_ubyte3_e32 v71, v142
	v_cvt_pk_fp8_f32 v58, v64, v59
	v_mul_f32_e32 v63, v65, v71
	v_mul_f32_e32 v62, 0x41800000, v62
	v_mul_f32_e32 v59, 0x41800000, v63
	v_cvt_f32_ubyte0_e32 v72, v143
	v_cvt_f32_ubyte1_e32 v73, v143
	v_med3_f32 v62, v62, s76, v237
	v_med3_f32 v59, v59, s76, v237
	v_cvt_pk_fp8_f32 v58, v62, v59 op_sel:[0,0,1]
	v_mul_f32_e32 v59, v66, v72
	v_mul_f32_e32 v62, v67, v73
	v_mul_f32_e32 v59, 0x41800000, v59
	v_mul_f32_e32 v62, 0x41800000, v62
	v_med3_f32 v63, v59, s76, v237
	v_med3_f32 v62, v62, s76, v237
	v_mov_b32_e32 v59, v1
	v_cvt_f32_ubyte2_e32 v74, v143
	v_cvt_f32_ubyte3_e32 v75, v143
	v_pk_mul_f32 v[60:61], v[60:61], s[88:89] op_sel_hi:[1,0]
	v_cvt_pk_fp8_f32 v59, v63, v62
	v_mul_f32_e32 v60, v60, v74
	v_mul_f32_e32 v61, v61, v75
	v_mul_f32_e32 v60, 0x41800000, v60
	v_mul_f32_e32 v61, 0x41800000, v61
	v_med3_f32 v60, v60, s76, v237
	v_med3_f32 v61, v61, s76, v237
	v_cvt_pk_fp8_f32 v59, v60, v61 op_sel:[0,0,1]
	v_cvt_f32_ubyte0_e32 v60, v144
	v_cvt_f32_ubyte1_e32 v61, v144
	v_cvt_f32_ubyte0_e32 v64, v145
	v_cvt_f32_ubyte1_e32 v65, v145
	v_pk_mul_f32 v[54:55], v[54:55], s[88:89] op_sel_hi:[1,0]
	v_pk_mul_f32 v[50:51], v[50:51], s[88:89] op_sel_hi:[1,0]
	v_mul_f32_e32 v54, v54, v60
	v_mul_f32_e32 v55, v55, v61
	v_mul_f32_e32 v50, v50, v64
	v_mul_f32_e32 v51, v51, v65
	v_mul_f32_e32 v54, 0x41800000, v54
	v_mul_f32_e32 v55, 0x41800000, v55
	v_mul_f32_e32 v50, 0x41800000, v50
	v_mul_f32_e32 v51, 0x41800000, v51
	v_med3_f32 v54, v54, s76, v237
	v_med3_f32 v55, v55, s76, v237
	v_mov_b32_e32 v60, v1
	v_med3_f32 v50, v50, s76, v237
	v_med3_f32 v51, v51, s76, v237
	v_mov_b32_e32 v61, v1
	v_cvt_f32_ubyte2_e32 v62, v144
	v_cvt_f32_ubyte3_e32 v63, v144
	v_cvt_f32_ubyte2_e32 v66, v145
	v_cvt_f32_ubyte3_e32 v67, v145
	v_pk_mul_f32 v[56:57], v[56:57], s[88:89] op_sel_hi:[1,0]
	v_pk_mul_f32 v[52:53], v[52:53], s[88:89] op_sel_hi:[1,0]
	v_cvt_pk_fp8_f32 v60, v54, v55
	v_cvt_pk_fp8_f32 v61, v50, v51
	v_mul_f32_e32 v56, v56, v62
	v_mul_f32_e32 v57, v57, v63
	v_mul_f32_e32 v52, v52, v66
	v_mul_f32_e32 v53, v53, v67
	v_mul_f32_e32 v56, 0x41800000, v56
	v_mul_f32_e32 v54, 0x41800000, v57
	v_mul_f32_e32 v52, 0x41800000, v52
	v_mul_f32_e32 v50, 0x41800000, v53
	v_med3_f32 v55, v56, s76, v237
	v_med3_f32 v54, v54, s76, v237
	v_med3_f32 v51, v52, s76, v237
	v_med3_f32 v50, v50, s76, v237
	v_ashrrev_i32_e32 v167, 31, v166
	v_cvt_pk_fp8_f32 v60, v55, v54 op_sel:[0,0,1]
	v_cvt_pk_fp8_f32 v61, v51, v50 op_sel:[0,0,1]
	v_lshlrev_b64 v[50:51], 11, v[166:167]
	v_lshl_add_u64 v[50:51], s[12:13], 0, v[50:51]
	v_lshl_add_u64 v[50:51], v[50:51], 0, v[158:159]
	s_waitcnt vmcnt(2)
	v_cvt_f32_ubyte0_e32 v52, v138
	v_cvt_f32_ubyte1_e32 v53, v138
	v_pk_mul_f32 v[46:47], v[46:47], s[88:89] op_sel_hi:[1,0]
	global_store_dwordx4 v[50:51], v[58:61], off
	v_pk_mul_f32 v[50:51], v[42:43], s[88:89] op_sel_hi:[1,0]
	v_mul_f32_e32 v42, v46, v52
	v_mul_f32_e32 v43, v47, v53
	v_cvt_f32_ubyte2_e32 v54, v138
	v_pk_mul_f32 v[48:49], v[48:49], s[88:89] op_sel_hi:[1,0]
	v_mul_f32_e32 v42, 0x41800000, v42
	v_mul_f32_e32 v43, 0x41800000, v43
	v_mul_f32_e32 v46, v48, v54
	v_med3_f32 v48, v42, s76, v237
	v_med3_f32 v43, v43, s76, v237
	v_mov_b32_e32 v42, v1
	v_cvt_f32_ubyte3_e32 v55, v138
	v_cvt_pk_fp8_f32 v42, v48, v43
	v_mul_f32_e32 v47, v49, v55
	v_mul_f32_e32 v46, 0x41800000, v46
	v_mul_f32_e32 v43, 0x41800000, v47
	v_cvt_f32_ubyte0_e32 v56, v139
	v_cvt_f32_ubyte1_e32 v57, v139
	v_med3_f32 v46, v46, s76, v237
	v_med3_f32 v43, v43, s76, v237
	v_cvt_pk_fp8_f32 v42, v46, v43 op_sel:[0,0,1]
	v_mul_f32_e32 v43, v50, v56
	v_mul_f32_e32 v46, v51, v57
	v_mul_f32_e32 v43, 0x41800000, v43
	v_mul_f32_e32 v46, 0x41800000, v46
	v_med3_f32 v47, v43, s76, v237
	v_med3_f32 v46, v46, s76, v237
	v_mov_b32_e32 v43, v1
	v_cvt_f32_ubyte2_e32 v58, v139
	v_cvt_f32_ubyte3_e32 v59, v139
	v_pk_mul_f32 v[44:45], v[44:45], s[88:89] op_sel_hi:[1,0]
	v_cvt_pk_fp8_f32 v43, v47, v46
	v_mul_f32_e32 v44, v44, v58
	v_mul_f32_e32 v45, v45, v59
	v_mul_f32_e32 v44, 0x41800000, v44
	v_mul_f32_e32 v45, 0x41800000, v45
	v_med3_f32 v44, v44, s76, v237
	v_med3_f32 v45, v45, s76, v237
	v_cvt_pk_fp8_f32 v43, v44, v45 op_sel:[0,0,1]
	v_cvt_f32_ubyte0_e32 v44, v140
	v_cvt_f32_ubyte1_e32 v45, v140
	v_cvt_f32_ubyte0_e32 v48, v141
	v_cvt_f32_ubyte1_e32 v49, v141
	v_pk_mul_f32 v[38:39], v[38:39], s[88:89] op_sel_hi:[1,0]
	v_pk_mul_f32 v[34:35], v[34:35], s[88:89] op_sel_hi:[1,0]
	v_mul_f32_e32 v38, v38, v44
	v_mul_f32_e32 v39, v39, v45
	v_mul_f32_e32 v34, v34, v48
	v_mul_f32_e32 v35, v35, v49
	v_mul_f32_e32 v38, 0x41800000, v38
	v_mul_f32_e32 v39, 0x41800000, v39
	v_mul_f32_e32 v34, 0x41800000, v34
	v_mul_f32_e32 v35, 0x41800000, v35
	v_med3_f32 v38, v38, s76, v237
	v_med3_f32 v39, v39, s76, v237
	v_mov_b32_e32 v44, v1
	v_med3_f32 v34, v34, s76, v237
	v_med3_f32 v35, v35, s76, v237
	v_mov_b32_e32 v45, v1
	v_cvt_f32_ubyte2_e32 v46, v140
	v_cvt_f32_ubyte3_e32 v47, v140
	v_cvt_f32_ubyte2_e32 v50, v141
	v_cvt_f32_ubyte3_e32 v51, v141
	v_pk_mul_f32 v[40:41], v[40:41], s[88:89] op_sel_hi:[1,0]
	v_pk_mul_f32 v[36:37], v[36:37], s[88:89] op_sel_hi:[1,0]
	v_cvt_pk_fp8_f32 v44, v38, v39
	v_cvt_pk_fp8_f32 v45, v34, v35
	v_mul_f32_e32 v40, v40, v46
	v_mul_f32_e32 v41, v41, v47
	v_mul_f32_e32 v36, v36, v50
	v_mul_f32_e32 v37, v37, v51
	v_mul_f32_e32 v40, 0x41800000, v40
	v_mul_f32_e32 v38, 0x41800000, v41
	v_mul_f32_e32 v36, 0x41800000, v36
	v_mul_f32_e32 v34, 0x41800000, v37
	v_med3_f32 v39, v40, s76, v237
	v_med3_f32 v38, v38, s76, v237
	v_med3_f32 v35, v36, s76, v237
	v_med3_f32 v34, v34, s76, v237
	v_ashrrev_i32_e32 v165, 31, v164
	v_cvt_pk_fp8_f32 v44, v39, v38 op_sel:[0,0,1]
	v_cvt_pk_fp8_f32 v45, v35, v34 op_sel:[0,0,1]
	v_lshlrev_b64 v[34:35], 11, v[164:165]
	v_lshl_add_u64 v[34:35], s[12:13], 0, v[34:35]
	v_lshl_add_u64 v[34:35], v[34:35], 0, v[158:159]
	s_waitcnt vmcnt(1)
	v_cvt_f32_ubyte0_e32 v36, v134
	v_cvt_f32_ubyte1_e32 v37, v134
	v_pk_mul_f32 v[30:31], v[30:31], s[88:89] op_sel_hi:[1,0]
	global_store_dwordx4 v[34:35], v[42:45], off
	v_pk_mul_f32 v[34:35], v[26:27], s[88:89] op_sel_hi:[1,0]
	v_mul_f32_e32 v26, v30, v36
	v_mul_f32_e32 v27, v31, v37
	v_cvt_f32_ubyte2_e32 v38, v134
	v_pk_mul_f32 v[32:33], v[32:33], s[88:89] op_sel_hi:[1,0]
	v_mul_f32_e32 v26, 0x41800000, v26
	v_mul_f32_e32 v27, 0x41800000, v27
	v_mul_f32_e32 v30, v32, v38
	v_med3_f32 v32, v26, s76, v237
	v_med3_f32 v27, v27, s76, v237
	v_mov_b32_e32 v26, v1
	v_cvt_f32_ubyte3_e32 v39, v134
	v_cvt_pk_fp8_f32 v26, v32, v27
	v_mul_f32_e32 v31, v33, v39
	v_mul_f32_e32 v30, 0x41800000, v30
	v_mul_f32_e32 v27, 0x41800000, v31
	v_cvt_f32_ubyte0_e32 v40, v135
	v_cvt_f32_ubyte1_e32 v41, v135
	v_med3_f32 v30, v30, s76, v237
	v_med3_f32 v27, v27, s76, v237
	v_cvt_pk_fp8_f32 v26, v30, v27 op_sel:[0,0,1]
	v_mul_f32_e32 v27, v34, v40
	v_mul_f32_e32 v30, v35, v41
	v_mul_f32_e32 v27, 0x41800000, v27
	v_mul_f32_e32 v30, 0x41800000, v30
	v_med3_f32 v31, v27, s76, v237
	v_med3_f32 v30, v30, s76, v237
	v_mov_b32_e32 v27, v1
	v_cvt_f32_ubyte2_e32 v42, v135
	v_cvt_f32_ubyte3_e32 v43, v135
	v_pk_mul_f32 v[28:29], v[28:29], s[88:89] op_sel_hi:[1,0]
	v_cvt_pk_fp8_f32 v27, v31, v30
	v_mul_f32_e32 v28, v28, v42
	v_mul_f32_e32 v29, v29, v43
	v_mul_f32_e32 v28, 0x41800000, v28
	v_mul_f32_e32 v29, 0x41800000, v29
	v_med3_f32 v28, v28, s76, v237
	v_med3_f32 v29, v29, s76, v237
	v_cvt_pk_fp8_f32 v27, v28, v29 op_sel:[0,0,1]
	v_cvt_f32_ubyte0_e32 v28, v136
	v_cvt_f32_ubyte1_e32 v29, v136
	v_cvt_f32_ubyte0_e32 v32, v137
	v_cvt_f32_ubyte1_e32 v33, v137
	v_pk_mul_f32 v[22:23], v[22:23], s[88:89] op_sel_hi:[1,0]
	v_pk_mul_f32 v[18:19], v[18:19], s[88:89] op_sel_hi:[1,0]
	v_mul_f32_e32 v22, v22, v28
	v_mul_f32_e32 v23, v23, v29
	v_mul_f32_e32 v18, v18, v32
	v_mul_f32_e32 v19, v19, v33
	v_mul_f32_e32 v22, 0x41800000, v22
	v_mul_f32_e32 v23, 0x41800000, v23
	v_mul_f32_e32 v18, 0x41800000, v18
	v_mul_f32_e32 v19, 0x41800000, v19
	v_med3_f32 v22, v22, s76, v237
	v_med3_f32 v23, v23, s76, v237
	v_mov_b32_e32 v28, v1
	v_med3_f32 v18, v18, s76, v237
	v_med3_f32 v19, v19, s76, v237
	v_mov_b32_e32 v29, v1
	v_cvt_f32_ubyte2_e32 v30, v136
	v_cvt_f32_ubyte3_e32 v31, v136
	v_cvt_f32_ubyte2_e32 v34, v137
	v_cvt_f32_ubyte3_e32 v35, v137
	v_pk_mul_f32 v[24:25], v[24:25], s[88:89] op_sel_hi:[1,0]
	v_pk_mul_f32 v[20:21], v[20:21], s[88:89] op_sel_hi:[1,0]
	v_cvt_pk_fp8_f32 v28, v22, v23
	v_cvt_pk_fp8_f32 v29, v18, v19
	v_mul_f32_e32 v24, v24, v30
	v_mul_f32_e32 v25, v25, v31
	v_mul_f32_e32 v20, v20, v34
	v_mul_f32_e32 v21, v21, v35
	v_mul_f32_e32 v24, 0x41800000, v24
	v_mul_f32_e32 v22, 0x41800000, v25
	v_mul_f32_e32 v20, 0x41800000, v20
	v_mul_f32_e32 v18, 0x41800000, v21
	v_med3_f32 v23, v24, s76, v237
	v_med3_f32 v22, v22, s76, v237
	v_med3_f32 v19, v20, s76, v237
	v_med3_f32 v18, v18, s76, v237
	v_ashrrev_i32_e32 v163, 31, v162
	v_cvt_pk_fp8_f32 v28, v23, v22 op_sel:[0,0,1]
	v_cvt_pk_fp8_f32 v29, v19, v18 op_sel:[0,0,1]
	v_lshlrev_b64 v[18:19], 11, v[162:163]
	v_lshl_add_u64 v[18:19], s[12:13], 0, v[18:19]
	v_lshl_add_u64 v[18:19], v[18:19], 0, v[158:159]
	global_store_dwordx4 v[18:19], v[26:29], off
	v_pk_mul_f32 v[14:15], v[14:15], s[88:89] op_sel_hi:[1,0]
	s_waitcnt vmcnt(0)
	v_cvt_f32_ubyte0_e32 v19, v130
	v_mul_f32_e32 v14, v14, v19
	v_mul_f32_e32 v14, 0x41800000, v14
	v_med3_f32 v19, v14, s76, v237
	v_cvt_f32_ubyte1_e32 v14, v130
	v_mul_f32_e32 v14, v15, v14
	v_mul_f32_e32 v14, 0x41800000, v14
	v_pk_mul_f32 v[16:17], v[16:17], s[88:89] op_sel_hi:[1,0]
	v_cvt_f32_ubyte2_e32 v18, v130
	v_med3_f32 v15, v14, s76, v237
	v_mov_b32_e32 v14, v1
	v_mul_f32_e32 v16, v16, v18
	v_cvt_f32_ubyte3_e32 v18, v130
	v_cvt_pk_fp8_f32 v14, v19, v15
	v_mul_f32_e32 v15, v17, v18
	v_mul_f32_e32 v16, 0x41800000, v16
	v_mul_f32_e32 v15, 0x41800000, v15
	v_med3_f32 v16, v16, s76, v237
	v_med3_f32 v15, v15, s76, v237
	v_cvt_pk_fp8_f32 v14, v16, v15 op_sel:[0,0,1]
	v_pk_mul_f32 v[12:13], v[12:13], s[88:89] op_sel_hi:[1,0]
	v_cvt_f32_ubyte2_e32 v15, v131
	v_pk_mul_f32 v[10:11], v[10:11], s[88:89] op_sel_hi:[1,0]
	v_mul_f32_e32 v12, v12, v15
	v_cvt_f32_ubyte0_e32 v15, v131
	v_mul_f32_e32 v10, v10, v15
	v_cvt_f32_ubyte1_e32 v15, v131
	v_mul_f32_e32 v11, v11, v15
	v_mul_f32_e32 v10, 0x41800000, v10
	v_mul_f32_e32 v11, 0x41800000, v11
	v_med3_f32 v10, v10, s76, v237
	v_med3_f32 v11, v11, s76, v237
	v_mov_b32_e32 v15, v1
	v_cvt_f32_ubyte3_e32 v16, v131
	v_cvt_pk_fp8_f32 v15, v10, v11
	v_mul_f32_e32 v10, v13, v16
	v_mul_f32_e32 v12, 0x41800000, v12
	v_mul_f32_e32 v10, 0x41800000, v10
	v_med3_f32 v12, v12, s76, v237
	v_med3_f32 v10, v10, s76, v237
	v_cvt_pk_fp8_f32 v15, v12, v10 op_sel:[0,0,1]
	v_cvt_f32_ubyte0_e32 v10, v132
	v_cvt_f32_ubyte1_e32 v11, v132
	v_cvt_f32_ubyte0_e32 v17, v133
	v_cvt_f32_ubyte1_e32 v18, v133
	v_pk_mul_f32 v[6:7], v[6:7], s[88:89] op_sel_hi:[1,0]
	v_pk_mul_f32 v[2:3], v[2:3], s[88:89] op_sel_hi:[1,0]
	v_mul_f32_e32 v6, v6, v10
	v_mul_f32_e32 v7, v7, v11
	v_mul_f32_e32 v2, v2, v17
	v_mul_f32_e32 v3, v3, v18
	v_mul_f32_e32 v6, 0x41800000, v6
	v_mul_f32_e32 v7, 0x41800000, v7
	v_mul_f32_e32 v2, 0x41800000, v2
	v_mul_f32_e32 v3, 0x41800000, v3
	v_med3_f32 v6, v6, s76, v237
	v_med3_f32 v7, v7, s76, v237
	v_mov_b32_e32 v16, v1
	v_med3_f32 v2, v2, s76, v237
	v_med3_f32 v3, v3, s76, v237
	v_mov_b32_e32 v17, v1
	v_cvt_f32_ubyte2_e32 v12, v132
	v_cvt_f32_ubyte3_e32 v13, v132
	v_cvt_f32_ubyte2_e32 v19, v133
	v_cvt_f32_ubyte3_e32 v20, v133
	v_pk_mul_f32 v[8:9], v[8:9], s[88:89] op_sel_hi:[1,0]
	v_pk_mul_f32 v[4:5], v[4:5], s[88:89] op_sel_hi:[1,0]
	v_cvt_pk_fp8_f32 v16, v6, v7
	v_cvt_pk_fp8_f32 v17, v2, v3
	v_mul_f32_e32 v8, v8, v12
	v_mul_f32_e32 v9, v9, v13
	v_mul_f32_e32 v4, v4, v19
	v_mul_f32_e32 v5, v5, v20
	v_mul_f32_e32 v8, 0x41800000, v8
	v_mul_f32_e32 v6, 0x41800000, v9
	v_mul_f32_e32 v4, 0x41800000, v4
	v_mul_f32_e32 v2, 0x41800000, v5
	v_med3_f32 v7, v8, s76, v237
	v_med3_f32 v6, v6, s76, v237
	v_med3_f32 v3, v4, s76, v237
	v_med3_f32 v2, v2, s76, v237
	v_ashrrev_i32_e32 v161, 31, v160
	v_cvt_pk_fp8_f32 v16, v7, v6 op_sel:[0,0,1]
	v_cvt_pk_fp8_f32 v17, v3, v2 op_sel:[0,0,1]
	v_lshlrev_b64 v[2:3], 11, v[160:161]
	v_lshl_add_u64 v[2:3], s[12:13], 0, v[2:3]
	v_lshl_add_u64 v[2:3], v[2:3], 0, v[158:159]
	s_andn2_b64 vcc, exec, s[2:3]
	s_mov_b64 s[2:3], -1
	global_store_dwordx4 v[2:3], v[14:17], off
	s_cbranch_vccnz .LBB0_3852
	s_andn2_b64 vcc, exec, s[8:9]
	s_cbranch_vccnz .LBB0_3851
	s_barrier
	s_branch .LBB0_3851
